# final_d + attention unit loop: counted wait vmcnt(2) at the loop top (do not wait for the last task's output store acknowledgements)
# speedup vs baseline: 1.0202x; 1.0093x over previous
.LBB0_258:
	s_cmp_lg_u32 s35, 0
	s_cselect_b64 s[66:67], -1, 0
	s_min_i32 s0, s3, 4
	s_add_i32 s2, s0, s20
	s_cmp_eq_u32 s35, 0
	s_cselect_b64 s[86:87], -1, 0
	s_and_b64 s[0:1], s[86:87], exec
	s_cselect_b32 s0, s2, 8
	s_waitcnt vmcnt(2)
	v_cvt_scalef32_pk_bf16_fp8 v4, v114, 1.0
	v_cvt_scalef32_pk_bf16_fp8 v5, v114, 1.0 op_sel:[1,0,0]
	v_cvt_scalef32_pk_bf16_fp8 v6, v115, 1.0
	v_cvt_scalef32_pk_bf16_fp8 v7, v115, 1.0 op_sel:[1,0,0]
	v_cvt_scalef32_pk_bf16_fp8 v8, v116, 1.0
	v_cvt_scalef32_pk_bf16_fp8 v9, v116, 1.0 op_sel:[1,0,0]
	v_cvt_scalef32_pk_bf16_fp8 v10, v117, 1.0
	v_cvt_scalef32_pk_bf16_fp8 v11, v117, 1.0 op_sel:[1,0,0]
	ds_write_b128 v196, v[4:7]
	ds_write_b128 v196, v[8:11] offset:16
	v_cvt_scalef32_pk_bf16_fp8 v4, v118, 1.0
	v_cvt_scalef32_pk_bf16_fp8 v5, v118, 1.0 op_sel:[1,0,0]
	v_cvt_scalef32_pk_bf16_fp8 v6, v119, 1.0
	v_cvt_scalef32_pk_bf16_fp8 v7, v119, 1.0 op_sel:[1,0,0]
	v_cvt_scalef32_pk_bf16_fp8 v8, v120, 1.0
	v_cvt_scalef32_pk_bf16_fp8 v9, v120, 1.0 op_sel:[1,0,0]
	v_cvt_scalef32_pk_bf16_fp8 v10, v121, 1.0
	v_cvt_scalef32_pk_bf16_fp8 v11, v121, 1.0 op_sel:[1,0,0]
	s_cmp_lt_i32 s0, 5
	ds_write_b128 v197, v[4:7]
	ds_write_b128 v197, v[8:11] offset:16
	s_cbranch_scc1 .LBB0_262
	v_cvt_scalef32_pk_bf16_fp8 v4, v122, 1.0
	v_cvt_scalef32_pk_bf16_fp8 v5, v122, 1.0 op_sel:[1,0,0]
	v_cvt_scalef32_pk_bf16_fp8 v6, v123, 1.0
	v_cvt_scalef32_pk_bf16_fp8 v7, v123, 1.0 op_sel:[1,0,0]
	v_cvt_scalef32_pk_bf16_fp8 v8, v124, 1.0
	v_cvt_scalef32_pk_bf16_fp8 v9, v124, 1.0 op_sel:[1,0,0]
	v_cvt_scalef32_pk_bf16_fp8 v10, v125, 1.0
	v_cvt_scalef32_pk_bf16_fp8 v11, v125, 1.0 op_sel:[1,0,0]
	ds_write_b128 v198, v[4:7]
	ds_write_b128 v198, v[8:11] offset:16
	s_cmp_lt_i32 s0, 7
	s_cbranch_scc0 .LBB0_263
